# gates GEMM: gate-bias vectors and the first three u rows of a unit requested at the top of the unit (before its K-loop) into registers free in the unit loop; epilogue copies instead of load+wait
# speedup vs baseline: 1.0017x; 1.0017x over previous
.LBB0_1269:
	s_lshl_b32 s6, s48, 6
	s_and_b32 s6, s6, 0xffffff80
	s_lshl_b32 s7, s48, 12
	s_and_b32 s7, s7, 0x1000
	v_add_u32_e32 v210, s6, v188
	v_ashrrev_i32_e32 v211, 31, v210
	v_lshlrev_b64 v[212:213], 2, v[210:211]
	s_add_u32 vcc_lo, s10, s7
	s_addc_u32 vcc_hi, s11, 0
	v_lshl_add_u64 v[214:215], vcc, 0, v[212:213]
	global_load_dwordx4 v[216:219], v[214:215], off offset:16
	global_load_dwordx4 v[220:223], v[214:215], off
	s_add_u32 vcc_lo, s12, s7
	s_addc_u32 vcc_hi, s13, 0
	v_lshl_add_u64 v[214:215], vcc, 0, v[212:213]
	global_load_dwordx4 v[224:227], v[214:215], off offset:16
	global_load_dwordx4 v[228:231], v[214:215], off
	s_add_u32 vcc_lo, s49, s7
	s_addc_u32 vcc_hi, s65, 0
	v_lshl_add_u64 v[214:215], vcc, 0, v[212:213]
	global_load_dwordx4 v[232:235], v[214:215], off
	global_load_dwordx4 v[236:239], v[214:215], off offset:16
	v_add_u32_e32 v214, s77, v186
	v_ashrrev_i32_e32 v215, 31, v214
	v_lshlrev_b64 v[214:215], 11, v[214:215]
	v_lshl_add_u64 v[214:215], s[8:9], 0, v[214:215]
	v_lshl_add_u64 v[214:215], v[210:211], 1, v[214:215]
	global_load_dwordx4 v[240:243], v[214:215], off
	v_add_co_u32_e32 v212, vcc, 0x8000, v214
	s_nop 1
	v_addc_co_u32_e32 v213, vcc, 0, v215, vcc
	global_load_dwordx4 v[244:247], v[212:213], off
	v_add_co_u32_e32 v212, vcc, 0x10000, v214
	s_nop 1
	v_addc_co_u32_e32 v213, vcc, 0, v215, vcc
	global_load_dwordx4 v[248:251], v[212:213], off
	s_mov_b32 s6, s68
	s_add_i32 s68, s68, 1
	s_cmp_gt_u32 s6, 0x3ffffffe
	s_mov_b64 s[40:41], 0
	s_cbranch_scc1 .LBB0_1277
	s_load_dword s28, s[90:91], 0x100
	s_mul_i32 s6, s68, s0
	s_waitcnt lgkmcnt(0)
	s_mul_hi_u32 s7, s68, s28
	s_add_i32 s7, s7, s6
	s_mul_i32 s6, s68, s28
	s_add_u32 s6, s6, s94
	s_addc_u32 s7, s7, s1
	v_cmp_gt_i64_e32 vcc, s[6:7], v[156:157]
	s_cbranch_vccnz .LBB0_1276
	s_ashr_i32 s7, s6, 31
	s_lshr_b32 s7, s7, 29
	s_add_i32 s7, s6, s7
	s_ashr_i32 s28, s7, 3
	s_and_b32 s7, s7, -8
	s_sub_i32 s6, s6, s7
	s_cmp_lt_i32 s6, 0
	s_movk_i32 s7, 0x121
	s_cselect_b32 s7, s7, 0x120
	s_mul_i32 s6, s7, s6
	s_add_i32 s6, s6, s28
	s_ashr_i32 s7, s6, 31
	s_lshr_b32 s7, s7, 25
	s_add_i32 s28, s6, s7
	s_ashr_i32 s7, s28, 7
	s_and_b32 s28, s28, 0xffffff80
	s_lshl_b32 s7, s7, 3
	s_sub_i32 s29, s6, s28
	s_cmpk_gt_i32 s6, 0x8ff
	s_mov_b64 s[30:31], -1
	s_cbranch_scc0 .LBB0_1273
	s_sub_i32 s6, 0x90, s7
	s_abs_i32 s28, s6
	v_cvt_f32_u32_e32 v0, s28
	s_sub_i32 s34, 0, s28
	s_abs_i32 s30, s29
	s_xor_b32 s31, s29, s6
	v_rcp_iflag_f32_e32 v0, v0
	s_ashr_i32 s31, s31, 31
	v_mul_f32_e32 v0, 0x4f7ffffe, v0
	v_cvt_u32_f32_e32 v0, v0
	s_nop 0
	v_readfirstlane_b32 s35, v0
	s_mul_i32 s34, s34, s35
	s_mul_hi_u32 s34, s35, s34
	s_add_i32 s35, s35, s34
	s_mul_hi_u32 s34, s30, s35
	s_mul_i32 s35, s34, s28
	s_sub_i32 s30, s30, s35
	s_add_i32 s36, s34, 1
	s_sub_i32 s35, s30, s28
	s_cmp_ge_u32 s30, s28
	s_cselect_b32 s34, s36, s34
	s_cselect_b32 s30, s35, s30
	s_add_i32 s35, s34, 1
	s_cmp_ge_u32 s30, s28
	s_cselect_b32 s28, s35, s34
	s_xor_b32 s28, s28, s31
	s_sub_i32 s28, s28, s31
	s_mul_i32 s6, s28, s6
	s_sub_i32 s6, s29, s6
	s_add_i32 s6, s6, s7
	s_mov_b64 s[30:31], 0

.LBB0_1284:
	s_lshl_b32 s52, s48, 6
	v_mov_b32_e32 v96, v188
	v_mov_b32_e32 v98, v186
	s_and_b32 s52, s52, 0xffffff80
	s_lshl_b32 s48, s48, 12
	s_and_b32 s48, s48, 0x1000
	v_add_u32_e32 v116, s52, v96
	s_waitcnt lgkmcnt(0)
	s_add_u32 s52, s10, s48
	v_ashrrev_i32_e32 v117, 31, v116
	s_addc_u32 s53, s11, 0
	v_lshlrev_b64 v[118:119], 2, v[116:117]
	v_lshl_add_u64 v[136:137], s[52:53], 0, v[118:119]
	s_add_u32 s52, s12, s48
	s_addc_u32 s53, s13, 0
	v_lshl_add_u64 v[136:137], s[52:53], 0, v[118:119]
	v_add_u32_e32 v136, s77, v98
	v_ashrrev_i32_e32 v137, 31, v136
	v_lshlrev_b64 v[136:137], 11, v[136:137]
	s_add_u32 s52, s49, s48
	v_lshl_add_u64 v[136:137], s[8:9], 0, v[136:137]
	s_addc_u32 s53, s65, 0
	v_ashrrev_i32_e32 v99, 31, v98
	v_lshl_add_u64 v[116:117], v[116:117], 1, v[136:137]
	v_lshl_add_u64 v[118:119], s[52:53], 0, v[118:119]
	v_lshlrev_b64 v[98:99], 13, v[98:99]
	s_mov_b32 s48, 0x8000
	v_ashrrev_i32_e32 v97, 31, v96
	v_lshl_add_u64 v[98:99], s[50:51], 0, v[98:99]
	v_lshl_add_u64 v[158:159], v[96:97], 1, v[98:99]
	v_add_co_u32_e32 v96, vcc, s48, v116
	s_mov_b32 s52, 0x10000
	s_nop 0
	v_addc_co_u32_e32 v97, vcc, 0, v117, vcc
	v_add_co_u32_e32 v98, vcc, s52, v116
	s_mov_b32 s53, 0x18000
	s_nop 0
	v_addc_co_u32_e32 v99, vcc, 0, v117, vcc
	v_add_co_u32_e32 v118, vcc, s53, v116
	s_mov_b32 s54, 0x48000
	s_nop 0
	v_addc_co_u32_e32 v119, vcc, 0, v117, vcc
	v_add_co_u32_e32 v136, vcc, s72, v116
	s_mov_b32 s55, 0x50000
	s_nop 0
	v_addc_co_u32_e32 v137, vcc, 0, v117, vcc
	v_add_co_u32_e32 v138, vcc, s54, v116
	s_mov_b32 s56, 0x58000
	s_nop 0
	v_addc_co_u32_e32 v139, vcc, 0, v117, vcc
	v_add_co_u32_e32 v168, vcc, s55, v116
	s_nop 1
	v_addc_co_u32_e32 v169, vcc, 0, v117, vcc
	v_add_co_u32_e32 v174, vcc, s56, v116
	s_nop 1
	v_addc_co_u32_e32 v175, vcc, 0, v117, vcc
	global_load_dwordx4 v[144:147], v[118:119], off
	global_load_dwordx4 v[140:143], v[136:137], off
	s_nop 0
	global_load_dwordx4 v[136:139], v[138:139], off
	s_nop 0
	global_load_dwordx4 v[116:119], v[168:169], off
	global_load_dwordx4 v[96:99], v[174:175], off
	s_waitcnt vmcnt(13)
	v_mov_b64_e32 v[160:161], v[216:217]
	v_mov_b64_e32 v[162:163], v[218:219]
	v_mov_b64_e32 v[164:165], v[220:221]
	v_mov_b64_e32 v[166:167], v[222:223]
	v_mov_b64_e32 v[192:193], v[224:225]
	v_mov_b64_e32 v[194:195], v[226:227]
	v_mov_b64_e32 v[170:171], v[228:229]
	v_mov_b64_e32 v[172:173], v[230:231]
	v_mov_b64_e32 v[200:201], v[232:233]
	v_mov_b64_e32 v[202:203], v[234:235]
	v_mov_b64_e32 v[204:205], v[236:237]
	v_mov_b64_e32 v[206:207], v[238:239]
	v_mov_b64_e32 v[196:197], v[240:241]
	v_mov_b64_e32 v[198:199], v[242:243]
	v_mov_b64_e32 v[152:153], v[244:245]
	v_mov_b64_e32 v[154:155], v[246:247]
	v_mov_b64_e32 v[148:149], v[248:249]
	v_mov_b64_e32 v[150:151], v[250:251]
	v_pk_mul_f32 v[162:163], v[162:163], s[20:21] op_sel_hi:[1,0]
	v_pk_mul_f32 v[176:177], v[170:171], s[20:21] op_sel_hi:[1,0]
	v_pk_mul_f32 v[174:175], v[166:167], s[20:21] op_sel_hi:[1,0]
	v_pk_mul_f32 v[168:169], v[160:161], s[20:21] op_sel_hi:[1,0]
	v_pk_fma_f32 v[134:135], v[134:135], s[22:23], v[174:175] op_sel_hi:[1,0,1] neg_lo:[1,0,0] neg_hi:[1,0,0]
	v_pk_fma_f32 v[128:129], v[128:129], s[22:23], v[176:177] op_sel_hi:[1,0,1] neg_lo:[1,0,0] neg_hi:[1,0,0]
	v_exp_f32_e32 v134, v134
	v_exp_f32_e32 v135, v135
	v_exp_f32_e32 v128, v128
	v_exp_f32_e32 v129, v129
	v_pk_fma_f32 v[124:125], v[124:125], s[22:23], v[168:169] op_sel_hi:[1,0,1] neg_lo:[1,0,0] neg_hi:[1,0,0]
	v_pk_add_f32 v[134:135], v[134:135], 1.0 op_sel_hi:[1,0]
	v_pk_mul_f32 v[180:181], v[164:165], s[20:21] op_sel_hi:[1,0]
	v_rcp_f32_e32 v134, v134
	v_rcp_f32_e32 v135, v135
	v_exp_f32_e32 v124, v124
	v_exp_f32_e32 v125, v125
	v_pk_fma_f32 v[126:127], v[126:127], s[22:23], v[162:163] op_sel_hi:[1,0,1] neg_lo:[1,0,0] neg_hi:[1,0,0]
	v_pk_fma_f32 v[208:209], v[132:133], s[22:23], v[180:181] op_sel_hi:[1,0,1] neg_lo:[1,0,0] neg_hi:[1,0,0]
	v_exp_f32_e32 v126, v126
	v_exp_f32_e32 v127, v127
	v_pk_mul_f32 v[170:171], v[172:173], s[20:21] op_sel_hi:[1,0]
	v_exp_f32_e32 v208, v208
	v_pk_mul_f32 v[172:173], v[202:203], s[22:23] op_sel_hi:[1,0]
	v_exp_f32_e32 v209, v209
	v_pk_add_f32 v[128:129], v[128:129], 1.0 op_sel_hi:[1,0]
	v_pk_fma_f32 v[130:131], v[130:131], s[22:23], v[170:171] op_sel_hi:[1,0,1] neg_lo:[1,0,0] neg_hi:[1,0,0]
	v_pk_mul_f32 v[134:135], v[172:173], v[134:135]
	v_rcp_f32_e32 v128, v128
	v_rcp_f32_e32 v129, v129
	v_exp_f32_e32 v130, v130
	v_exp_f32_e32 v131, v131
	v_exp_f32_e32 v134, v134
	v_exp_f32_e32 v135, v135
	v_pk_add_f32 v[124:125], v[124:125], 1.0 op_sel_hi:[1,0]
	v_pk_add_f32 v[126:127], v[126:127], 1.0 op_sel_hi:[1,0]
	v_rcp_f32_e32 v124, v124
	v_rcp_f32_e32 v125, v125
	v_pk_mul_f32 v[178:179], v[200:201], s[22:23] op_sel_hi:[1,0]
	v_pk_add_f32 v[200:201], v[208:209], 1.0 op_sel_hi:[1,0]
	v_rcp_f32_e32 v126, v126
	v_rcp_f32_e32 v127, v127
	v_pk_mul_f32 v[164:165], v[192:193], s[20:21] op_sel_hi:[1,0]
	v_lshlrev_b32_e32 v192, 16, v196
	v_and_b32_e32 v193, 0xffff0000, v196
	v_rcp_f32_e32 v200, v200
	v_rcp_f32_e32 v201, v201
	v_pk_mul_f32 v[166:167], v[204:205], s[22:23] op_sel_hi:[1,0]
	v_pk_mul_f32 v[128:129], v[128:129], v[192:193]
	v_pk_add_f32 v[130:131], v[130:131], 1.0 op_sel_hi:[1,0]
	v_pk_add_f32 v[192:193], v[134:135], 1.0 op_sel_hi:[1,0] neg_lo:[1,0] neg_hi:[1,0]
	v_pk_add_f32 v[134:135], v[134:135], 1.0 op_sel_hi:[1,0]
	v_pk_mul_f32 v[160:161], v[194:195], s[20:21] op_sel_hi:[1,0]
	v_pk_mul_f32 v[132:133], v[206:207], s[22:23] op_sel_hi:[1,0]
	v_rcp_f32_e32 v130, v130
	v_rcp_f32_e32 v131, v131
	v_pk_mul_f32 v[134:135], v[192:193], v[134:135]
	v_pk_fma_f32 v[120:121], v[120:121], s[22:23], v[164:165] op_sel_hi:[1,0,1] neg_lo:[1,0,0] neg_hi:[1,0,0]
	v_pk_mul_f32 v[124:125], v[166:167], v[124:125]
	v_sqrt_f32_e32 v134, v134
	v_sqrt_f32_e32 v135, v135
	v_exp_f32_e32 v120, v120
	v_exp_f32_e32 v121, v121
	v_exp_f32_e32 v124, v124
	v_exp_f32_e32 v125, v125
	v_pk_fma_f32 v[122:123], v[122:123], s[22:23], v[160:161] op_sel_hi:[1,0,1] neg_lo:[1,0,0] neg_hi:[1,0,0]
	v_pk_mul_f32 v[126:127], v[132:133], v[126:127]
	v_pk_mul_f32 v[200:201], v[178:179], v[200:201]
	v_exp_f32_e32 v122, v122
	v_exp_f32_e32 v123, v123
	v_exp_f32_e32 v126, v126
	v_exp_f32_e32 v127, v127
	v_lshlrev_b32_e32 v194, 16, v197
	v_and_b32_e32 v195, 0xffff0000, v197
	v_exp_f32_e32 v200, v200
	v_exp_f32_e32 v201, v201
	v_pk_mul_f32 v[130:131], v[130:131], v[194:195]
	v_pk_add_f32 v[120:121], v[120:121], 1.0 op_sel_hi:[1,0]
	v_pk_mul_f32 v[130:131], v[130:131], v[134:135]
	v_pk_add_f32 v[134:135], v[124:125], 1.0 op_sel_hi:[1,0] neg_lo:[1,0] neg_hi:[1,0]
	v_pk_add_f32 v[124:125], v[124:125], 1.0 op_sel_hi:[1,0]
	v_rcp_f32_e32 v120, v120
	v_rcp_f32_e32 v121, v121
	v_pk_mul_f32 v[124:125], v[134:135], v[124:125]
	v_pk_add_f32 v[122:123], v[122:123], 1.0 op_sel_hi:[1,0]
	v_pk_add_f32 v[194:195], v[126:127], 1.0 op_sel_hi:[1,0] neg_lo:[1,0] neg_hi:[1,0]
	v_pk_add_f32 v[126:127], v[126:127], 1.0 op_sel_hi:[1,0]
	v_pk_add_f32 v[202:203], v[200:201], 1.0 op_sel_hi:[1,0] neg_lo:[1,0] neg_hi:[1,0]
	v_pk_add_f32 v[200:201], v[200:201], 1.0 op_sel_hi:[1,0]
	v_sqrt_f32_e32 v124, v124
	v_sqrt_f32_e32 v125, v125
	v_rcp_f32_e32 v122, v122
	v_rcp_f32_e32 v123, v123
	v_pk_mul_f32 v[126:127], v[194:195], v[126:127]
	v_pk_mul_f32 v[200:201], v[202:203], v[200:201]
	v_sqrt_f32_e32 v126, v126
	v_sqrt_f32_e32 v127, v127
	v_lshlrev_b32_e32 v196, 16, v198
	v_and_b32_e32 v197, 0xffff0000, v198
	v_sqrt_f32_e32 v200, v200
	v_sqrt_f32_e32 v201, v201
	v_lshlrev_b32_e32 v198, 16, v199
	v_and_b32_e32 v199, 0xffff0000, v199
	v_pk_mul_f32 v[120:121], v[120:121], v[196:197]
	v_pk_mul_f32 v[128:129], v[128:129], v[200:201]
	v_pk_mul_f32 v[124:125], v[120:121], v[124:125]
	v_pk_mul_f32 v[120:121], v[122:123], v[198:199]
	v_cvt_pk_bf16_f32 v122, v134, v135
	v_cvt_pk_bf16_f32 v123, v194, v195
	s_nop 0
	v_pk_mul_f32 v[126:127], v[120:121], v[126:127]
	v_cvt_pk_bf16_f32 v120, v202, v203
	v_cvt_pk_bf16_f32 v121, v192, v193
	global_store_dwordx4 v[158:159], v[120:123], off
	s_nop 1
	v_cvt_pk_bf16_f32 v120, v128, v129
	v_cvt_pk_bf16_f32 v121, v130, v131
	v_cvt_pk_bf16_f32 v122, v124, v125
	v_cvt_pk_bf16_f32 v123, v126, v127
	global_store_dwordx4 v[158:159], v[120:123], off offset:256
	v_pk_fma_f32 v[112:113], v[112:113], s[22:23], v[180:181] op_sel_hi:[1,0,1] neg_lo:[1,0,0] neg_hi:[1,0,0]
	v_pk_fma_f32 v[114:115], v[114:115], s[22:23], v[174:175] op_sel_hi:[1,0,1] neg_lo:[1,0,0] neg_hi:[1,0,0]
	v_exp_f32_e32 v112, v112
	v_exp_f32_e32 v113, v113
	v_exp_f32_e32 v114, v114
	v_exp_f32_e32 v115, v115
	v_pk_fma_f32 v[108:109], v[108:109], s[22:23], v[176:177] op_sel_hi:[1,0,1] neg_lo:[1,0,0] neg_hi:[1,0,0]
	v_pk_add_f32 v[112:113], v[112:113], 1.0 op_sel_hi:[1,0]
	v_pk_fma_f32 v[104:105], v[104:105], s[22:23], v[168:169] op_sel_hi:[1,0,1] neg_lo:[1,0,0] neg_hi:[1,0,0]
	v_rcp_f32_e32 v112, v112
	v_rcp_f32_e32 v113, v113
	v_pk_add_f32 v[114:115], v[114:115], 1.0 op_sel_hi:[1,0]
	v_exp_f32_e32 v108, v108
	v_exp_f32_e32 v109, v109
	v_rcp_f32_e32 v114, v114
	v_rcp_f32_e32 v115, v115
	v_exp_f32_e32 v104, v104
	v_exp_f32_e32 v105, v105
	v_pk_fma_f32 v[106:107], v[106:107], s[22:23], v[162:163] op_sel_hi:[1,0,1] neg_lo:[1,0,0] neg_hi:[1,0,0]
	v_pk_mul_f32 v[112:113], v[178:179], v[112:113]
	v_exp_f32_e32 v106, v106
	v_exp_f32_e32 v107, v107
	v_exp_f32_e32 v112, v112
	v_exp_f32_e32 v113, v113
	v_pk_add_f32 v[108:109], v[108:109], 1.0 op_sel_hi:[1,0]
	v_pk_fma_f32 v[110:111], v[110:111], s[22:23], v[170:171] op_sel_hi:[1,0,1] neg_lo:[1,0,0] neg_hi:[1,0,0]
	v_pk_mul_f32 v[114:115], v[172:173], v[114:115]
	v_pk_add_f32 v[104:105], v[104:105], 1.0 op_sel_hi:[1,0]
	v_rcp_f32_e32 v108, v108
	v_rcp_f32_e32 v109, v109
	v_exp_f32_e32 v110, v110
	v_exp_f32_e32 v111, v111
	v_exp_f32_e32 v114, v114
	v_exp_f32_e32 v115, v115
	v_rcp_f32_e32 v104, v104
	v_rcp_f32_e32 v105, v105
	v_pk_add_f32 v[106:107], v[106:107], 1.0 op_sel_hi:[1,0]
	v_lshlrev_b32_e32 v120, 16, v152
	v_rcp_f32_e32 v106, v106
	v_rcp_f32_e32 v107, v107
	v_and_b32_e32 v121, 0xffff0000, v152
	v_pk_add_f32 v[128:129], v[112:113], 1.0 op_sel_hi:[1,0] neg_lo:[1,0] neg_hi:[1,0]
	v_pk_add_f32 v[112:113], v[112:113], 1.0 op_sel_hi:[1,0]
	v_pk_mul_f32 v[108:109], v[108:109], v[120:121]
	v_pk_mul_f32 v[112:113], v[128:129], v[112:113]
	v_pk_add_f32 v[110:111], v[110:111], 1.0 op_sel_hi:[1,0]
	v_pk_add_f32 v[120:121], v[114:115], 1.0 op_sel_hi:[1,0] neg_lo:[1,0] neg_hi:[1,0]
	v_pk_add_f32 v[114:115], v[114:115], 1.0 op_sel_hi:[1,0]
	v_pk_fma_f32 v[100:101], v[100:101], s[22:23], v[164:165] op_sel_hi:[1,0,1] neg_lo:[1,0,0] neg_hi:[1,0,0]
	v_pk_mul_f32 v[104:105], v[166:167], v[104:105]
	v_sqrt_f32_e32 v112, v112
	v_sqrt_f32_e32 v113, v113
	v_rcp_f32_e32 v110, v110
	v_rcp_f32_e32 v111, v111
	v_pk_mul_f32 v[114:115], v[120:121], v[114:115]
	v_exp_f32_e32 v100, v100
	v_exp_f32_e32 v101, v101
	v_exp_f32_e32 v104, v104
	v_exp_f32_e32 v105, v105
	v_pk_fma_f32 v[102:103], v[102:103], s[22:23], v[160:161] op_sel_hi:[1,0,1] neg_lo:[1,0,0] neg_hi:[1,0,0]
	v_pk_mul_f32 v[106:107], v[132:133], v[106:107]
	v_sqrt_f32_e32 v114, v114
	v_sqrt_f32_e32 v115, v115
	v_exp_f32_e32 v102, v102
	v_exp_f32_e32 v103, v103
	v_exp_f32_e32 v106, v106
	v_exp_f32_e32 v107, v107
	v_lshlrev_b32_e32 v122, 16, v153
	v_and_b32_e32 v123, 0xffff0000, v153
	v_pk_mul_f32 v[108:109], v[108:109], v[112:113]
	v_pk_mul_f32 v[110:111], v[110:111], v[122:123]
	v_pk_add_f32 v[100:101], v[100:101], 1.0 op_sel_hi:[1,0]
	v_pk_add_f32 v[112:113], v[104:105], 1.0 op_sel_hi:[1,0] neg_lo:[1,0] neg_hi:[1,0]
	v_pk_add_f32 v[104:105], v[104:105], 1.0 op_sel_hi:[1,0]
	v_pk_mul_f32 v[110:111], v[110:111], v[114:115]
	v_rcp_f32_e32 v100, v100
	v_rcp_f32_e32 v101, v101
	v_pk_mul_f32 v[104:105], v[112:113], v[104:105]
	v_pk_add_f32 v[102:103], v[102:103], 1.0 op_sel_hi:[1,0]
	v_pk_add_f32 v[114:115], v[106:107], 1.0 op_sel_hi:[1,0] neg_lo:[1,0] neg_hi:[1,0]
	v_pk_add_f32 v[106:107], v[106:107], 1.0 op_sel_hi:[1,0]
	v_sqrt_f32_e32 v104, v104
	v_sqrt_f32_e32 v105, v105
	v_rcp_f32_e32 v102, v102
	v_rcp_f32_e32 v103, v103
	v_pk_mul_f32 v[106:107], v[114:115], v[106:107]
	v_lshlrev_b32_e32 v124, 16, v154
	v_sqrt_f32_e32 v106, v106
	v_sqrt_f32_e32 v107, v107
	v_and_b32_e32 v125, 0xffff0000, v154
	v_lshlrev_b32_e32 v126, 16, v155
	v_and_b32_e32 v127, 0xffff0000, v155
	v_pk_mul_f32 v[100:101], v[100:101], v[124:125]
	s_mov_b32 s48, 0x20000
	v_pk_mul_f32 v[104:105], v[100:101], v[104:105]
	v_pk_mul_f32 v[100:101], v[102:103], v[126:127]
	v_cvt_pk_bf16_f32 v102, v112, v113
	v_add_co_u32_e32 v112, vcc, s48, v158
	v_pk_mul_f32 v[106:107], v[100:101], v[106:107]
	v_cvt_pk_bf16_f32 v100, v128, v129
	v_cvt_pk_bf16_f32 v101, v120, v121
	v_cvt_pk_bf16_f32 v103, v114, v115
	s_nop 0
	v_addc_co_u32_e32 v113, vcc, 0, v159, vcc
	global_store_dwordx4 v[112:113], v[100:103], off
	s_nop 1
	v_cvt_pk_bf16_f32 v100, v108, v109
	v_cvt_pk_bf16_f32 v101, v110, v111
	v_cvt_pk_bf16_f32 v102, v104, v105
	v_cvt_pk_bf16_f32 v103, v106, v107
	global_store_dwordx4 v[112:113], v[100:103], off offset:256
	v_pk_fma_f32 v[92:93], v[92:93], s[22:23], v[180:181] op_sel_hi:[1,0,1] neg_lo:[1,0,0] neg_hi:[1,0,0]
	v_pk_fma_f32 v[94:95], v[94:95], s[22:23], v[174:175] op_sel_hi:[1,0,1] neg_lo:[1,0,0] neg_hi:[1,0,0]
	v_exp_f32_e32 v92, v92
	v_exp_f32_e32 v93, v93
	v_exp_f32_e32 v94, v94
	v_exp_f32_e32 v95, v95
	v_pk_fma_f32 v[88:89], v[88:89], s[22:23], v[176:177] op_sel_hi:[1,0,1] neg_lo:[1,0,0] neg_hi:[1,0,0]
	v_pk_add_f32 v[92:93], v[92:93], 1.0 op_sel_hi:[1,0]
	v_pk_fma_f32 v[84:85], v[84:85], s[22:23], v[168:169] op_sel_hi:[1,0,1] neg_lo:[1,0,0] neg_hi:[1,0,0]
	v_rcp_f32_e32 v92, v92
	v_rcp_f32_e32 v93, v93
	v_pk_add_f32 v[94:95], v[94:95], 1.0 op_sel_hi:[1,0]
	v_exp_f32_e32 v88, v88
	v_exp_f32_e32 v89, v89
	v_rcp_f32_e32 v94, v94
	v_rcp_f32_e32 v95, v95
	v_exp_f32_e32 v84, v84
	v_exp_f32_e32 v85, v85
	v_pk_fma_f32 v[86:87], v[86:87], s[22:23], v[162:163] op_sel_hi:[1,0,1] neg_lo:[1,0,0] neg_hi:[1,0,0]
	v_pk_mul_f32 v[92:93], v[178:179], v[92:93]
	v_exp_f32_e32 v86, v86
	v_exp_f32_e32 v87, v87
	v_exp_f32_e32 v92, v92
	v_exp_f32_e32 v93, v93
	v_pk_add_f32 v[88:89], v[88:89], 1.0 op_sel_hi:[1,0]
	v_pk_fma_f32 v[90:91], v[90:91], s[22:23], v[170:171] op_sel_hi:[1,0,1] neg_lo:[1,0,0] neg_hi:[1,0,0]
	v_pk_mul_f32 v[94:95], v[172:173], v[94:95]
	v_pk_add_f32 v[84:85], v[84:85], 1.0 op_sel_hi:[1,0]
	v_rcp_f32_e32 v88, v88
	v_rcp_f32_e32 v89, v89
	v_exp_f32_e32 v90, v90
	v_exp_f32_e32 v91, v91
	v_exp_f32_e32 v94, v94
	v_exp_f32_e32 v95, v95
	v_rcp_f32_e32 v84, v84
	v_rcp_f32_e32 v85, v85
	v_pk_add_f32 v[86:87], v[86:87], 1.0 op_sel_hi:[1,0]
	v_lshlrev_b32_e32 v100, 16, v148
	v_rcp_f32_e32 v86, v86
	v_rcp_f32_e32 v87, v87
	v_and_b32_e32 v101, 0xffff0000, v148
	v_pk_add_f32 v[108:109], v[92:93], 1.0 op_sel_hi:[1,0] neg_lo:[1,0] neg_hi:[1,0]
	v_pk_add_f32 v[92:93], v[92:93], 1.0 op_sel_hi:[1,0]
	v_pk_mul_f32 v[88:89], v[88:89], v[100:101]
	v_pk_mul_f32 v[92:93], v[108:109], v[92:93]
	v_pk_add_f32 v[90:91], v[90:91], 1.0 op_sel_hi:[1,0]
	v_pk_add_f32 v[100:101], v[94:95], 1.0 op_sel_hi:[1,0] neg_lo:[1,0] neg_hi:[1,0]
	v_pk_add_f32 v[94:95], v[94:95], 1.0 op_sel_hi:[1,0]
	v_pk_fma_f32 v[80:81], v[80:81], s[22:23], v[164:165] op_sel_hi:[1,0,1] neg_lo:[1,0,0] neg_hi:[1,0,0]
	v_pk_mul_f32 v[84:85], v[166:167], v[84:85]
	v_sqrt_f32_e32 v92, v92
	v_sqrt_f32_e32 v93, v93
	v_rcp_f32_e32 v90, v90
	v_rcp_f32_e32 v91, v91
	v_pk_mul_f32 v[94:95], v[100:101], v[94:95]
	v_exp_f32_e32 v80, v80
	v_exp_f32_e32 v81, v81
	v_exp_f32_e32 v84, v84
	v_exp_f32_e32 v85, v85
	v_pk_fma_f32 v[82:83], v[82:83], s[22:23], v[160:161] op_sel_hi:[1,0,1] neg_lo:[1,0,0] neg_hi:[1,0,0]
	v_pk_mul_f32 v[86:87], v[132:133], v[86:87]
	v_sqrt_f32_e32 v94, v94
	v_sqrt_f32_e32 v95, v95
	v_exp_f32_e32 v82, v82
	v_exp_f32_e32 v83, v83
	v_exp_f32_e32 v86, v86
	v_exp_f32_e32 v87, v87
	v_lshlrev_b32_e32 v102, 16, v149
	v_and_b32_e32 v103, 0xffff0000, v149
	v_pk_mul_f32 v[88:89], v[88:89], v[92:93]
	v_pk_mul_f32 v[90:91], v[90:91], v[102:103]
	v_pk_add_f32 v[80:81], v[80:81], 1.0 op_sel_hi:[1,0]
	v_pk_add_f32 v[92:93], v[84:85], 1.0 op_sel_hi:[1,0] neg_lo:[1,0] neg_hi:[1,0]
	v_pk_add_f32 v[84:85], v[84:85], 1.0 op_sel_hi:[1,0]
	v_pk_mul_f32 v[90:91], v[90:91], v[94:95]
	v_rcp_f32_e32 v80, v80
	v_rcp_f32_e32 v81, v81
	v_pk_mul_f32 v[84:85], v[92:93], v[84:85]
	v_pk_add_f32 v[82:83], v[82:83], 1.0 op_sel_hi:[1,0]
	v_pk_add_f32 v[94:95], v[86:87], 1.0 op_sel_hi:[1,0] neg_lo:[1,0] neg_hi:[1,0]
	v_pk_add_f32 v[86:87], v[86:87], 1.0 op_sel_hi:[1,0]
	v_sqrt_f32_e32 v84, v84
	v_sqrt_f32_e32 v85, v85
	v_rcp_f32_e32 v82, v82
	v_rcp_f32_e32 v83, v83
	v_pk_mul_f32 v[86:87], v[94:95], v[86:87]
	v_lshlrev_b32_e32 v104, 16, v150
	v_sqrt_f32_e32 v86, v86
	v_sqrt_f32_e32 v87, v87
	v_and_b32_e32 v105, 0xffff0000, v150
	v_lshlrev_b32_e32 v106, 16, v151
	v_and_b32_e32 v107, 0xffff0000, v151
	v_pk_mul_f32 v[80:81], v[80:81], v[104:105]
	s_nop 0
	v_pk_mul_f32 v[84:85], v[80:81], v[84:85]
	v_pk_mul_f32 v[80:81], v[82:83], v[106:107]
	v_cvt_pk_bf16_f32 v82, v92, v93
	v_add_co_u32_e32 v92, vcc, s72, v158
	v_pk_mul_f32 v[86:87], v[80:81], v[86:87]
	v_cvt_pk_bf16_f32 v80, v108, v109
	v_cvt_pk_bf16_f32 v81, v100, v101
	v_cvt_pk_bf16_f32 v83, v94, v95
	s_nop 0
	v_addc_co_u32_e32 v93, vcc, 0, v159, vcc
	global_store_dwordx4 v[92:93], v[80:83], off
	s_nop 1
	v_cvt_pk_bf16_f32 v80, v88, v89
	v_cvt_pk_bf16_f32 v81, v90, v91
	v_cvt_pk_bf16_f32 v82, v84, v85
	v_cvt_pk_bf16_f32 v83, v86, v87
	global_store_dwordx4 v[92:93], v[80:83], off offset:256
	v_pk_fma_f32 v[76:77], v[76:77], s[22:23], v[180:181] op_sel_hi:[1,0,1] neg_lo:[1,0,0] neg_hi:[1,0,0]
	v_pk_fma_f32 v[78:79], v[78:79], s[22:23], v[174:175] op_sel_hi:[1,0,1] neg_lo:[1,0,0] neg_hi:[1,0,0]
	v_exp_f32_e32 v76, v76
	v_exp_f32_e32 v77, v77
	v_exp_f32_e32 v78, v78
	v_exp_f32_e32 v79, v79
	v_pk_fma_f32 v[72:73], v[72:73], s[22:23], v[176:177] op_sel_hi:[1,0,1] neg_lo:[1,0,0] neg_hi:[1,0,0]
	v_pk_add_f32 v[76:77], v[76:77], 1.0 op_sel_hi:[1,0]
	v_pk_fma_f32 v[68:69], v[68:69], s[22:23], v[168:169] op_sel_hi:[1,0,1] neg_lo:[1,0,0] neg_hi:[1,0,0]
	v_rcp_f32_e32 v76, v76
	v_rcp_f32_e32 v77, v77
	v_pk_add_f32 v[78:79], v[78:79], 1.0 op_sel_hi:[1,0]
	v_exp_f32_e32 v72, v72
	v_exp_f32_e32 v73, v73
	v_rcp_f32_e32 v78, v78
	v_rcp_f32_e32 v79, v79
	v_exp_f32_e32 v68, v68
	v_exp_f32_e32 v69, v69
	v_pk_fma_f32 v[70:71], v[70:71], s[22:23], v[162:163] op_sel_hi:[1,0,1] neg_lo:[1,0,0] neg_hi:[1,0,0]
	v_pk_mul_f32 v[76:77], v[178:179], v[76:77]
	v_exp_f32_e32 v70, v70
	v_exp_f32_e32 v71, v71
	v_exp_f32_e32 v76, v76
	v_exp_f32_e32 v77, v77
	v_pk_add_f32 v[72:73], v[72:73], 1.0 op_sel_hi:[1,0]
	v_pk_fma_f32 v[74:75], v[74:75], s[22:23], v[170:171] op_sel_hi:[1,0,1] neg_lo:[1,0,0] neg_hi:[1,0,0]
	v_pk_mul_f32 v[78:79], v[172:173], v[78:79]
	v_pk_add_f32 v[68:69], v[68:69], 1.0 op_sel_hi:[1,0]
	v_rcp_f32_e32 v72, v72
	v_rcp_f32_e32 v73, v73
	v_exp_f32_e32 v74, v74
	v_exp_f32_e32 v75, v75
	v_exp_f32_e32 v78, v78
	v_exp_f32_e32 v79, v79
	v_rcp_f32_e32 v68, v68
	v_rcp_f32_e32 v69, v69
	v_pk_add_f32 v[70:71], v[70:71], 1.0 op_sel_hi:[1,0]
	s_waitcnt vmcnt(10)
	v_lshlrev_b32_e32 v80, 16, v144
	v_rcp_f32_e32 v70, v70
	v_rcp_f32_e32 v71, v71
	v_and_b32_e32 v81, 0xffff0000, v144
	v_pk_add_f32 v[88:89], v[76:77], 1.0 op_sel_hi:[1,0] neg_lo:[1,0] neg_hi:[1,0]
	v_pk_add_f32 v[76:77], v[76:77], 1.0 op_sel_hi:[1,0]
	v_pk_mul_f32 v[72:73], v[72:73], v[80:81]
	v_pk_mul_f32 v[76:77], v[88:89], v[76:77]
	v_pk_add_f32 v[74:75], v[74:75], 1.0 op_sel_hi:[1,0]
	v_pk_add_f32 v[80:81], v[78:79], 1.0 op_sel_hi:[1,0] neg_lo:[1,0] neg_hi:[1,0]
	v_pk_add_f32 v[78:79], v[78:79], 1.0 op_sel_hi:[1,0]
	v_pk_fma_f32 v[64:65], v[64:65], s[22:23], v[164:165] op_sel_hi:[1,0,1] neg_lo:[1,0,0] neg_hi:[1,0,0]
	v_pk_mul_f32 v[68:69], v[166:167], v[68:69]
	v_sqrt_f32_e32 v76, v76
	v_sqrt_f32_e32 v77, v77
	v_rcp_f32_e32 v74, v74
	v_rcp_f32_e32 v75, v75
	v_pk_mul_f32 v[78:79], v[80:81], v[78:79]
	v_exp_f32_e32 v64, v64
	v_exp_f32_e32 v65, v65
	v_exp_f32_e32 v68, v68
	v_exp_f32_e32 v69, v69
	v_pk_fma_f32 v[66:67], v[66:67], s[22:23], v[160:161] op_sel_hi:[1,0,1] neg_lo:[1,0,0] neg_hi:[1,0,0]
	v_pk_mul_f32 v[70:71], v[132:133], v[70:71]
	v_sqrt_f32_e32 v78, v78
	v_sqrt_f32_e32 v79, v79
	v_exp_f32_e32 v66, v66
	v_exp_f32_e32 v67, v67
	v_exp_f32_e32 v70, v70
	v_exp_f32_e32 v71, v71
	v_lshlrev_b32_e32 v82, 16, v145
	v_and_b32_e32 v83, 0xffff0000, v145
	v_pk_mul_f32 v[72:73], v[72:73], v[76:77]
	v_pk_mul_f32 v[74:75], v[74:75], v[82:83]
	v_pk_add_f32 v[64:65], v[64:65], 1.0 op_sel_hi:[1,0]
	v_pk_add_f32 v[76:77], v[68:69], 1.0 op_sel_hi:[1,0] neg_lo:[1,0] neg_hi:[1,0]
	v_pk_add_f32 v[68:69], v[68:69], 1.0 op_sel_hi:[1,0]
	v_pk_mul_f32 v[74:75], v[74:75], v[78:79]
	v_rcp_f32_e32 v64, v64
	v_rcp_f32_e32 v65, v65
	v_pk_mul_f32 v[68:69], v[76:77], v[68:69]
	v_pk_add_f32 v[66:67], v[66:67], 1.0 op_sel_hi:[1,0]
	v_pk_add_f32 v[78:79], v[70:71], 1.0 op_sel_hi:[1,0] neg_lo:[1,0] neg_hi:[1,0]
	v_pk_add_f32 v[70:71], v[70:71], 1.0 op_sel_hi:[1,0]
	v_sqrt_f32_e32 v68, v68
	v_sqrt_f32_e32 v69, v69
	v_rcp_f32_e32 v66, v66
	v_rcp_f32_e32 v67, v67
	v_pk_mul_f32 v[70:71], v[78:79], v[70:71]
	v_lshlrev_b32_e32 v84, 16, v146
	v_sqrt_f32_e32 v70, v70
	v_sqrt_f32_e32 v71, v71
	v_and_b32_e32 v85, 0xffff0000, v146
	v_lshlrev_b32_e32 v86, 16, v147
	v_and_b32_e32 v87, 0xffff0000, v147
	v_pk_mul_f32 v[64:65], v[64:65], v[84:85]
	s_nop 0
	v_pk_mul_f32 v[68:69], v[64:65], v[68:69]
	v_pk_mul_f32 v[64:65], v[66:67], v[86:87]
	v_cvt_pk_bf16_f32 v66, v76, v77
	v_add_co_u32_e32 v76, vcc, s73, v158
	v_pk_mul_f32 v[70:71], v[64:65], v[70:71]
	v_cvt_pk_bf16_f32 v64, v88, v89
	v_cvt_pk_bf16_f32 v65, v80, v81
	v_cvt_pk_bf16_f32 v67, v78, v79
	s_nop 0
	v_addc_co_u32_e32 v77, vcc, 0, v159, vcc
	global_store_dwordx4 v[76:77], v[64:67], off
	s_nop 1
	v_cvt_pk_bf16_f32 v64, v72, v73
	v_cvt_pk_bf16_f32 v65, v74, v75
	v_cvt_pk_bf16_f32 v66, v68, v69
	v_cvt_pk_bf16_f32 v67, v70, v71
	global_store_dwordx4 v[76:77], v[64:67], off offset:256
	v_pk_fma_f32 v[60:61], v[60:61], s[22:23], v[180:181] op_sel_hi:[1,0,1] neg_lo:[1,0,0] neg_hi:[1,0,0]
	v_pk_fma_f32 v[62:63], v[62:63], s[22:23], v[174:175] op_sel_hi:[1,0,1] neg_lo:[1,0,0] neg_hi:[1,0,0]
	v_exp_f32_e32 v60, v60
	v_exp_f32_e32 v61, v61
	v_exp_f32_e32 v62, v62
	v_exp_f32_e32 v63, v63
	v_pk_fma_f32 v[56:57], v[56:57], s[22:23], v[176:177] op_sel_hi:[1,0,1] neg_lo:[1,0,0] neg_hi:[1,0,0]
	v_pk_add_f32 v[60:61], v[60:61], 1.0 op_sel_hi:[1,0]
	v_pk_fma_f32 v[52:53], v[52:53], s[22:23], v[168:169] op_sel_hi:[1,0,1] neg_lo:[1,0,0] neg_hi:[1,0,0]
	v_rcp_f32_e32 v60, v60
	v_rcp_f32_e32 v61, v61
	v_pk_add_f32 v[62:63], v[62:63], 1.0 op_sel_hi:[1,0]
	v_exp_f32_e32 v56, v56
	v_exp_f32_e32 v57, v57
	v_rcp_f32_e32 v62, v62
	v_rcp_f32_e32 v63, v63
	v_exp_f32_e32 v52, v52
	v_exp_f32_e32 v53, v53
	v_pk_fma_f32 v[54:55], v[54:55], s[22:23], v[162:163] op_sel_hi:[1,0,1] neg_lo:[1,0,0] neg_hi:[1,0,0]
	v_pk_mul_f32 v[60:61], v[178:179], v[60:61]
	v_exp_f32_e32 v54, v54
	v_exp_f32_e32 v55, v55
	v_exp_f32_e32 v60, v60
	v_exp_f32_e32 v61, v61
	v_pk_add_f32 v[56:57], v[56:57], 1.0 op_sel_hi:[1,0]
	v_pk_fma_f32 v[58:59], v[58:59], s[22:23], v[170:171] op_sel_hi:[1,0,1] neg_lo:[1,0,0] neg_hi:[1,0,0]
	v_pk_mul_f32 v[62:63], v[172:173], v[62:63]
	v_pk_add_f32 v[52:53], v[52:53], 1.0 op_sel_hi:[1,0]
	v_rcp_f32_e32 v56, v56
	v_rcp_f32_e32 v57, v57
	v_exp_f32_e32 v58, v58
	v_exp_f32_e32 v59, v59
	v_exp_f32_e32 v62, v62
	v_exp_f32_e32 v63, v63
	v_rcp_f32_e32 v52, v52
	v_rcp_f32_e32 v53, v53
	v_pk_add_f32 v[54:55], v[54:55], 1.0 op_sel_hi:[1,0]
	s_waitcnt vmcnt(11)
	v_lshlrev_b32_e32 v64, 16, v140
	v_rcp_f32_e32 v54, v54
	v_rcp_f32_e32 v55, v55
	v_and_b32_e32 v65, 0xffff0000, v140
	v_pk_add_f32 v[72:73], v[60:61], 1.0 op_sel_hi:[1,0] neg_lo:[1,0] neg_hi:[1,0]
	v_pk_add_f32 v[60:61], v[60:61], 1.0 op_sel_hi:[1,0]
	v_pk_mul_f32 v[56:57], v[56:57], v[64:65]
	v_pk_mul_f32 v[60:61], v[72:73], v[60:61]
	v_pk_add_f32 v[58:59], v[58:59], 1.0 op_sel_hi:[1,0]
	v_pk_add_f32 v[64:65], v[62:63], 1.0 op_sel_hi:[1,0] neg_lo:[1,0] neg_hi:[1,0]
	v_pk_add_f32 v[62:63], v[62:63], 1.0 op_sel_hi:[1,0]
	v_pk_fma_f32 v[48:49], v[48:49], s[22:23], v[164:165] op_sel_hi:[1,0,1] neg_lo:[1,0,0] neg_hi:[1,0,0]
	v_pk_mul_f32 v[52:53], v[166:167], v[52:53]
	v_sqrt_f32_e32 v60, v60
	v_sqrt_f32_e32 v61, v61
	v_rcp_f32_e32 v58, v58
	v_rcp_f32_e32 v59, v59
	v_pk_mul_f32 v[62:63], v[64:65], v[62:63]
	v_exp_f32_e32 v48, v48
	v_exp_f32_e32 v49, v49
	v_exp_f32_e32 v52, v52
	v_exp_f32_e32 v53, v53
	v_pk_fma_f32 v[50:51], v[50:51], s[22:23], v[160:161] op_sel_hi:[1,0,1] neg_lo:[1,0,0] neg_hi:[1,0,0]
	v_pk_mul_f32 v[54:55], v[132:133], v[54:55]
	v_sqrt_f32_e32 v62, v62
	v_sqrt_f32_e32 v63, v63
	v_exp_f32_e32 v50, v50
	v_exp_f32_e32 v51, v51
	v_exp_f32_e32 v54, v54
	v_exp_f32_e32 v55, v55
	v_lshlrev_b32_e32 v66, 16, v141
	v_and_b32_e32 v67, 0xffff0000, v141
	v_pk_mul_f32 v[56:57], v[56:57], v[60:61]
	v_pk_mul_f32 v[58:59], v[58:59], v[66:67]
	v_pk_add_f32 v[48:49], v[48:49], 1.0 op_sel_hi:[1,0]
	v_pk_add_f32 v[60:61], v[52:53], 1.0 op_sel_hi:[1,0] neg_lo:[1,0] neg_hi:[1,0]
	v_pk_add_f32 v[52:53], v[52:53], 1.0 op_sel_hi:[1,0]
	v_pk_mul_f32 v[58:59], v[58:59], v[62:63]
	v_rcp_f32_e32 v48, v48
	v_rcp_f32_e32 v49, v49
	v_pk_mul_f32 v[52:53], v[60:61], v[52:53]
	v_pk_add_f32 v[50:51], v[50:51], 1.0 op_sel_hi:[1,0]
	v_pk_add_f32 v[62:63], v[54:55], 1.0 op_sel_hi:[1,0] neg_lo:[1,0] neg_hi:[1,0]
	v_pk_add_f32 v[54:55], v[54:55], 1.0 op_sel_hi:[1,0]
	v_sqrt_f32_e32 v52, v52
	v_sqrt_f32_e32 v53, v53
	v_rcp_f32_e32 v50, v50
	v_rcp_f32_e32 v51, v51
	v_pk_mul_f32 v[54:55], v[62:63], v[54:55]
	v_lshlrev_b32_e32 v68, 16, v142
	v_sqrt_f32_e32 v54, v54
	v_sqrt_f32_e32 v55, v55
	v_and_b32_e32 v69, 0xffff0000, v142
	v_lshlrev_b32_e32 v70, 16, v143
	v_and_b32_e32 v71, 0xffff0000, v143
	v_pk_mul_f32 v[48:49], v[48:49], v[68:69]
	s_nop 0
	v_pk_mul_f32 v[52:53], v[48:49], v[52:53]
	v_pk_mul_f32 v[48:49], v[50:51], v[70:71]
	v_cvt_pk_bf16_f32 v50, v60, v61
	v_add_co_u32_e32 v60, vcc, s74, v158
	v_pk_mul_f32 v[54:55], v[48:49], v[54:55]
	v_cvt_pk_bf16_f32 v48, v72, v73
	v_cvt_pk_bf16_f32 v49, v64, v65
	v_cvt_pk_bf16_f32 v51, v62, v63
	s_nop 0
	v_addc_co_u32_e32 v61, vcc, 0, v159, vcc
	global_store_dwordx4 v[60:61], v[48:51], off
	s_nop 1
	v_cvt_pk_bf16_f32 v48, v56, v57
	v_cvt_pk_bf16_f32 v49, v58, v59
	v_cvt_pk_bf16_f32 v50, v52, v53
	v_cvt_pk_bf16_f32 v51, v54, v55
	global_store_dwordx4 v[60:61], v[48:51], off offset:256
	v_pk_fma_f32 v[44:45], v[44:45], s[22:23], v[180:181] op_sel_hi:[1,0,1] neg_lo:[1,0,0] neg_hi:[1,0,0]
	v_pk_fma_f32 v[46:47], v[46:47], s[22:23], v[174:175] op_sel_hi:[1,0,1] neg_lo:[1,0,0] neg_hi:[1,0,0]
	v_exp_f32_e32 v44, v44
	v_exp_f32_e32 v45, v45
	v_exp_f32_e32 v46, v46
	v_exp_f32_e32 v47, v47
	v_pk_fma_f32 v[40:41], v[40:41], s[22:23], v[176:177] op_sel_hi:[1,0,1] neg_lo:[1,0,0] neg_hi:[1,0,0]
	v_pk_add_f32 v[44:45], v[44:45], 1.0 op_sel_hi:[1,0]
	v_pk_fma_f32 v[36:37], v[36:37], s[22:23], v[168:169] op_sel_hi:[1,0,1] neg_lo:[1,0,0] neg_hi:[1,0,0]
	v_rcp_f32_e32 v44, v44
	v_rcp_f32_e32 v45, v45
	v_pk_add_f32 v[46:47], v[46:47], 1.0 op_sel_hi:[1,0]
	v_exp_f32_e32 v40, v40
	v_exp_f32_e32 v41, v41
	v_rcp_f32_e32 v46, v46
	v_rcp_f32_e32 v47, v47
	v_exp_f32_e32 v36, v36
	v_exp_f32_e32 v37, v37
	v_pk_fma_f32 v[38:39], v[38:39], s[22:23], v[162:163] op_sel_hi:[1,0,1] neg_lo:[1,0,0] neg_hi:[1,0,0]
	v_pk_mul_f32 v[44:45], v[178:179], v[44:45]
	v_exp_f32_e32 v38, v38
	v_exp_f32_e32 v39, v39
	v_exp_f32_e32 v44, v44
	v_exp_f32_e32 v45, v45
	v_pk_add_f32 v[40:41], v[40:41], 1.0 op_sel_hi:[1,0]
	v_pk_fma_f32 v[42:43], v[42:43], s[22:23], v[170:171] op_sel_hi:[1,0,1] neg_lo:[1,0,0] neg_hi:[1,0,0]
	v_pk_mul_f32 v[46:47], v[172:173], v[46:47]
	v_pk_add_f32 v[36:37], v[36:37], 1.0 op_sel_hi:[1,0]
	v_rcp_f32_e32 v40, v40
	v_rcp_f32_e32 v41, v41
	v_exp_f32_e32 v42, v42
	v_exp_f32_e32 v43, v43
	v_exp_f32_e32 v46, v46
	v_exp_f32_e32 v47, v47
	v_rcp_f32_e32 v36, v36
	v_rcp_f32_e32 v37, v37
	v_pk_add_f32 v[38:39], v[38:39], 1.0 op_sel_hi:[1,0]
	s_waitcnt vmcnt(12)
	v_lshlrev_b32_e32 v48, 16, v136
	v_rcp_f32_e32 v38, v38
	v_rcp_f32_e32 v39, v39
	v_and_b32_e32 v49, 0xffff0000, v136
	v_pk_add_f32 v[56:57], v[44:45], 1.0 op_sel_hi:[1,0] neg_lo:[1,0] neg_hi:[1,0]
	v_pk_add_f32 v[44:45], v[44:45], 1.0 op_sel_hi:[1,0]
	v_pk_mul_f32 v[40:41], v[40:41], v[48:49]
	v_pk_mul_f32 v[44:45], v[56:57], v[44:45]
	v_pk_add_f32 v[42:43], v[42:43], 1.0 op_sel_hi:[1,0]
	v_pk_add_f32 v[48:49], v[46:47], 1.0 op_sel_hi:[1,0] neg_lo:[1,0] neg_hi:[1,0]
	v_pk_add_f32 v[46:47], v[46:47], 1.0 op_sel_hi:[1,0]
	v_pk_fma_f32 v[32:33], v[32:33], s[22:23], v[164:165] op_sel_hi:[1,0,1] neg_lo:[1,0,0] neg_hi:[1,0,0]
	v_pk_mul_f32 v[36:37], v[166:167], v[36:37]
	v_sqrt_f32_e32 v44, v44
	v_sqrt_f32_e32 v45, v45
	v_rcp_f32_e32 v42, v42
	v_rcp_f32_e32 v43, v43
	v_pk_mul_f32 v[46:47], v[48:49], v[46:47]
	v_exp_f32_e32 v32, v32
	v_exp_f32_e32 v33, v33
	v_exp_f32_e32 v36, v36
	v_exp_f32_e32 v37, v37
	v_pk_fma_f32 v[34:35], v[34:35], s[22:23], v[160:161] op_sel_hi:[1,0,1] neg_lo:[1,0,0] neg_hi:[1,0,0]
	v_pk_mul_f32 v[38:39], v[132:133], v[38:39]
	v_sqrt_f32_e32 v46, v46
	v_sqrt_f32_e32 v47, v47
	v_exp_f32_e32 v34, v34
	v_exp_f32_e32 v35, v35
	v_exp_f32_e32 v38, v38
	v_exp_f32_e32 v39, v39
	v_lshlrev_b32_e32 v50, 16, v137
	v_and_b32_e32 v51, 0xffff0000, v137
	v_pk_mul_f32 v[40:41], v[40:41], v[44:45]
	v_pk_mul_f32 v[42:43], v[42:43], v[50:51]
	v_pk_add_f32 v[32:33], v[32:33], 1.0 op_sel_hi:[1,0]
	v_pk_add_f32 v[44:45], v[36:37], 1.0 op_sel_hi:[1,0] neg_lo:[1,0] neg_hi:[1,0]
	v_pk_add_f32 v[36:37], v[36:37], 1.0 op_sel_hi:[1,0]
	v_pk_mul_f32 v[42:43], v[42:43], v[46:47]
	v_rcp_f32_e32 v32, v32
	v_rcp_f32_e32 v33, v33
	v_pk_mul_f32 v[36:37], v[44:45], v[36:37]
	v_pk_add_f32 v[34:35], v[34:35], 1.0 op_sel_hi:[1,0]
	v_pk_add_f32 v[46:47], v[38:39], 1.0 op_sel_hi:[1,0] neg_lo:[1,0] neg_hi:[1,0]
	v_pk_add_f32 v[38:39], v[38:39], 1.0 op_sel_hi:[1,0]
	v_sqrt_f32_e32 v36, v36
	v_sqrt_f32_e32 v37, v37
	v_rcp_f32_e32 v34, v34
	v_rcp_f32_e32 v35, v35
	v_pk_mul_f32 v[38:39], v[46:47], v[38:39]
	v_lshlrev_b32_e32 v52, 16, v138
	v_sqrt_f32_e32 v38, v38
	v_sqrt_f32_e32 v39, v39
	v_and_b32_e32 v53, 0xffff0000, v138
	v_lshlrev_b32_e32 v54, 16, v139
	v_and_b32_e32 v55, 0xffff0000, v139
	v_pk_mul_f32 v[32:33], v[32:33], v[52:53]
	s_nop 0
	v_pk_mul_f32 v[36:37], v[32:33], v[36:37]
	v_pk_mul_f32 v[32:33], v[34:35], v[54:55]
	v_cvt_pk_bf16_f32 v34, v44, v45
	v_add_co_u32_e32 v44, vcc, s75, v158
	v_pk_mul_f32 v[38:39], v[32:33], v[38:39]
	v_cvt_pk_bf16_f32 v32, v56, v57
	v_cvt_pk_bf16_f32 v33, v48, v49
	v_cvt_pk_bf16_f32 v35, v46, v47
	s_nop 0
	v_addc_co_u32_e32 v45, vcc, 0, v159, vcc
	global_store_dwordx4 v[44:45], v[32:35], off
	s_nop 1
	v_cvt_pk_bf16_f32 v32, v40, v41
	v_cvt_pk_bf16_f32 v33, v42, v43
	v_cvt_pk_bf16_f32 v34, v36, v37
	v_cvt_pk_bf16_f32 v35, v38, v39
	global_store_dwordx4 v[44:45], v[32:35], off offset:256
	v_pk_fma_f32 v[28:29], v[28:29], s[22:23], v[180:181] op_sel_hi:[1,0,1] neg_lo:[1,0,0] neg_hi:[1,0,0]
	v_pk_fma_f32 v[30:31], v[30:31], s[22:23], v[174:175] op_sel_hi:[1,0,1] neg_lo:[1,0,0] neg_hi:[1,0,0]
	v_exp_f32_e32 v28, v28
	v_exp_f32_e32 v29, v29
	v_exp_f32_e32 v30, v30
	v_exp_f32_e32 v31, v31
	v_pk_fma_f32 v[24:25], v[24:25], s[22:23], v[176:177] op_sel_hi:[1,0,1] neg_lo:[1,0,0] neg_hi:[1,0,0]
	v_pk_add_f32 v[28:29], v[28:29], 1.0 op_sel_hi:[1,0]
	v_pk_fma_f32 v[20:21], v[20:21], s[22:23], v[168:169] op_sel_hi:[1,0,1] neg_lo:[1,0,0] neg_hi:[1,0,0]
	v_rcp_f32_e32 v28, v28
	v_rcp_f32_e32 v29, v29
	v_pk_add_f32 v[30:31], v[30:31], 1.0 op_sel_hi:[1,0]
	v_exp_f32_e32 v24, v24
	v_exp_f32_e32 v25, v25
	v_rcp_f32_e32 v30, v30
	v_rcp_f32_e32 v31, v31
	v_exp_f32_e32 v20, v20
	v_exp_f32_e32 v21, v21
	v_pk_fma_f32 v[22:23], v[22:23], s[22:23], v[162:163] op_sel_hi:[1,0,1] neg_lo:[1,0,0] neg_hi:[1,0,0]
	v_pk_mul_f32 v[28:29], v[178:179], v[28:29]
	v_exp_f32_e32 v22, v22
	v_exp_f32_e32 v23, v23
	v_exp_f32_e32 v28, v28
	v_exp_f32_e32 v29, v29
	v_pk_add_f32 v[24:25], v[24:25], 1.0 op_sel_hi:[1,0]
	v_pk_fma_f32 v[26:27], v[26:27], s[22:23], v[170:171] op_sel_hi:[1,0,1] neg_lo:[1,0,0] neg_hi:[1,0,0]
	v_pk_mul_f32 v[30:31], v[172:173], v[30:31]
	v_pk_add_f32 v[20:21], v[20:21], 1.0 op_sel_hi:[1,0]
	v_rcp_f32_e32 v24, v24
	v_rcp_f32_e32 v25, v25
	v_exp_f32_e32 v26, v26
	v_exp_f32_e32 v27, v27
	v_exp_f32_e32 v30, v30
	v_exp_f32_e32 v31, v31
	v_rcp_f32_e32 v20, v20
	v_rcp_f32_e32 v21, v21
	v_pk_add_f32 v[22:23], v[22:23], 1.0 op_sel_hi:[1,0]
	s_waitcnt vmcnt(13)
	v_lshlrev_b32_e32 v32, 16, v116
	v_rcp_f32_e32 v22, v22
	v_rcp_f32_e32 v23, v23
	v_and_b32_e32 v33, 0xffff0000, v116
	v_pk_add_f32 v[40:41], v[28:29], 1.0 op_sel_hi:[1,0] neg_lo:[1,0] neg_hi:[1,0]
	v_pk_add_f32 v[28:29], v[28:29], 1.0 op_sel_hi:[1,0]
	v_pk_mul_f32 v[24:25], v[24:25], v[32:33]
	v_pk_mul_f32 v[28:29], v[40:41], v[28:29]
	v_pk_add_f32 v[26:27], v[26:27], 1.0 op_sel_hi:[1,0]
	v_pk_add_f32 v[32:33], v[30:31], 1.0 op_sel_hi:[1,0] neg_lo:[1,0] neg_hi:[1,0]
	v_pk_add_f32 v[30:31], v[30:31], 1.0 op_sel_hi:[1,0]
	v_pk_fma_f32 v[16:17], v[16:17], s[22:23], v[164:165] op_sel_hi:[1,0,1] neg_lo:[1,0,0] neg_hi:[1,0,0]
	v_pk_mul_f32 v[20:21], v[166:167], v[20:21]
	v_sqrt_f32_e32 v28, v28
	v_sqrt_f32_e32 v29, v29
	v_rcp_f32_e32 v26, v26
	v_rcp_f32_e32 v27, v27
	v_pk_mul_f32 v[30:31], v[32:33], v[30:31]
	v_exp_f32_e32 v16, v16
	v_exp_f32_e32 v17, v17
	v_exp_f32_e32 v20, v20
	v_exp_f32_e32 v21, v21
	v_pk_fma_f32 v[18:19], v[18:19], s[22:23], v[160:161] op_sel_hi:[1,0,1] neg_lo:[1,0,0] neg_hi:[1,0,0]
	v_pk_mul_f32 v[22:23], v[132:133], v[22:23]
	v_sqrt_f32_e32 v30, v30
	v_sqrt_f32_e32 v31, v31
	v_exp_f32_e32 v18, v18
	v_exp_f32_e32 v19, v19
	v_exp_f32_e32 v22, v22
	v_exp_f32_e32 v23, v23
	v_lshlrev_b32_e32 v34, 16, v117
	v_and_b32_e32 v35, 0xffff0000, v117
	v_pk_mul_f32 v[24:25], v[24:25], v[28:29]
	v_pk_mul_f32 v[26:27], v[26:27], v[34:35]
	v_pk_add_f32 v[16:17], v[16:17], 1.0 op_sel_hi:[1,0]
	v_pk_add_f32 v[28:29], v[20:21], 1.0 op_sel_hi:[1,0] neg_lo:[1,0] neg_hi:[1,0]
	v_pk_add_f32 v[20:21], v[20:21], 1.0 op_sel_hi:[1,0]
	v_pk_mul_f32 v[26:27], v[26:27], v[30:31]
	v_rcp_f32_e32 v16, v16
	v_rcp_f32_e32 v17, v17
	v_pk_mul_f32 v[20:21], v[28:29], v[20:21]
	v_pk_add_f32 v[18:19], v[18:19], 1.0 op_sel_hi:[1,0]
	v_pk_add_f32 v[30:31], v[22:23], 1.0 op_sel_hi:[1,0] neg_lo:[1,0] neg_hi:[1,0]
	v_pk_add_f32 v[22:23], v[22:23], 1.0 op_sel_hi:[1,0]
	v_sqrt_f32_e32 v20, v20
	v_sqrt_f32_e32 v21, v21
	v_rcp_f32_e32 v18, v18
	v_rcp_f32_e32 v19, v19
	v_pk_mul_f32 v[22:23], v[30:31], v[22:23]
	v_lshlrev_b32_e32 v36, 16, v118
	v_sqrt_f32_e32 v22, v22
	v_sqrt_f32_e32 v23, v23
	v_and_b32_e32 v37, 0xffff0000, v118
	v_lshlrev_b32_e32 v38, 16, v119
	v_and_b32_e32 v39, 0xffff0000, v119
	v_pk_mul_f32 v[16:17], v[16:17], v[36:37]
	s_nop 0
	v_pk_mul_f32 v[20:21], v[16:17], v[20:21]
	v_pk_mul_f32 v[16:17], v[18:19], v[38:39]
	v_cvt_pk_bf16_f32 v18, v28, v29
	v_add_co_u32_e32 v28, vcc, s76, v158
	v_pk_mul_f32 v[22:23], v[16:17], v[22:23]
	v_cvt_pk_bf16_f32 v16, v40, v41
	v_cvt_pk_bf16_f32 v17, v32, v33
	v_cvt_pk_bf16_f32 v19, v30, v31
	s_nop 0
	v_addc_co_u32_e32 v29, vcc, 0, v159, vcc
	global_store_dwordx4 v[28:29], v[16:19], off
	s_nop 1
	v_cvt_pk_bf16_f32 v16, v24, v25
	v_cvt_pk_bf16_f32 v17, v26, v27
	v_cvt_pk_bf16_f32 v18, v20, v21
	v_cvt_pk_bf16_f32 v19, v22, v23
	global_store_dwordx4 v[28:29], v[16:19], off offset:256
	v_pk_fma_f32 v[12:13], v[12:13], s[22:23], v[180:181] op_sel_hi:[1,0,1] neg_lo:[1,0,0] neg_hi:[1,0,0]
	v_pk_fma_f32 v[14:15], v[14:15], s[22:23], v[174:175] op_sel_hi:[1,0,1] neg_lo:[1,0,0] neg_hi:[1,0,0]
	v_exp_f32_e32 v12, v12
	v_exp_f32_e32 v13, v13
	v_exp_f32_e32 v14, v14
	v_exp_f32_e32 v15, v15
	v_pk_fma_f32 v[8:9], v[8:9], s[22:23], v[176:177] op_sel_hi:[1,0,1] neg_lo:[1,0,0] neg_hi:[1,0,0]
	v_pk_add_f32 v[12:13], v[12:13], 1.0 op_sel_hi:[1,0]
	v_pk_fma_f32 v[4:5], v[4:5], s[22:23], v[168:169] op_sel_hi:[1,0,1] neg_lo:[1,0,0] neg_hi:[1,0,0]
	v_rcp_f32_e32 v12, v12
	v_rcp_f32_e32 v13, v13
	v_pk_add_f32 v[14:15], v[14:15], 1.0 op_sel_hi:[1,0]
	v_exp_f32_e32 v8, v8
	v_exp_f32_e32 v9, v9
	v_rcp_f32_e32 v14, v14
	v_rcp_f32_e32 v15, v15
	v_exp_f32_e32 v4, v4
	v_exp_f32_e32 v5, v5
	v_pk_fma_f32 v[6:7], v[6:7], s[22:23], v[162:163] op_sel_hi:[1,0,1] neg_lo:[1,0,0] neg_hi:[1,0,0]
	v_pk_mul_f32 v[12:13], v[178:179], v[12:13]
	v_exp_f32_e32 v6, v6
	v_exp_f32_e32 v7, v7
	v_exp_f32_e32 v12, v12
	v_exp_f32_e32 v13, v13
	v_pk_add_f32 v[8:9], v[8:9], 1.0 op_sel_hi:[1,0]
	v_pk_fma_f32 v[10:11], v[10:11], s[22:23], v[170:171] op_sel_hi:[1,0,1] neg_lo:[1,0,0] neg_hi:[1,0,0]
	v_pk_mul_f32 v[14:15], v[172:173], v[14:15]
	v_pk_add_f32 v[4:5], v[4:5], 1.0 op_sel_hi:[1,0]
	v_rcp_f32_e32 v8, v8
	v_rcp_f32_e32 v9, v9
	v_exp_f32_e32 v10, v10
	v_exp_f32_e32 v11, v11
	v_exp_f32_e32 v14, v14
	v_exp_f32_e32 v15, v15
	v_rcp_f32_e32 v4, v4
	v_rcp_f32_e32 v5, v5
	v_pk_add_f32 v[6:7], v[6:7], 1.0 op_sel_hi:[1,0]
	s_waitcnt vmcnt(14)
	v_lshlrev_b32_e32 v16, 16, v96
	v_rcp_f32_e32 v6, v6
	v_rcp_f32_e32 v7, v7
	v_and_b32_e32 v17, 0xffff0000, v96
	v_pk_add_f32 v[24:25], v[12:13], 1.0 op_sel_hi:[1,0] neg_lo:[1,0] neg_hi:[1,0]
	v_pk_add_f32 v[12:13], v[12:13], 1.0 op_sel_hi:[1,0]
	v_pk_mul_f32 v[8:9], v[8:9], v[16:17]
	v_pk_mul_f32 v[12:13], v[24:25], v[12:13]
	v_pk_add_f32 v[10:11], v[10:11], 1.0 op_sel_hi:[1,0]
	v_pk_add_f32 v[16:17], v[14:15], 1.0 op_sel_hi:[1,0] neg_lo:[1,0] neg_hi:[1,0]
	v_pk_add_f32 v[14:15], v[14:15], 1.0 op_sel_hi:[1,0]
	v_pk_fma_f32 v[0:1], v[0:1], s[22:23], v[164:165] op_sel_hi:[1,0,1] neg_lo:[1,0,0] neg_hi:[1,0,0]
	v_pk_mul_f32 v[4:5], v[166:167], v[4:5]
	v_sqrt_f32_e32 v12, v12
	v_sqrt_f32_e32 v13, v13
	v_rcp_f32_e32 v10, v10
	v_rcp_f32_e32 v11, v11
	v_pk_mul_f32 v[14:15], v[16:17], v[14:15]
	v_exp_f32_e32 v0, v0
	v_exp_f32_e32 v1, v1
	v_exp_f32_e32 v4, v4
	v_exp_f32_e32 v5, v5
	v_pk_fma_f32 v[2:3], v[2:3], s[22:23], v[160:161] op_sel_hi:[1,0,1] neg_lo:[1,0,0] neg_hi:[1,0,0]
	v_pk_mul_f32 v[6:7], v[132:133], v[6:7]
	v_sqrt_f32_e32 v14, v14
	v_sqrt_f32_e32 v15, v15
	v_exp_f32_e32 v2, v2
	v_exp_f32_e32 v3, v3
	v_exp_f32_e32 v6, v6
	v_exp_f32_e32 v7, v7
	v_lshlrev_b32_e32 v18, 16, v97
	v_and_b32_e32 v19, 0xffff0000, v97
	v_pk_mul_f32 v[8:9], v[8:9], v[12:13]
	v_pk_mul_f32 v[10:11], v[10:11], v[18:19]
	v_pk_add_f32 v[0:1], v[0:1], 1.0 op_sel_hi:[1,0]
	v_pk_add_f32 v[12:13], v[4:5], 1.0 op_sel_hi:[1,0] neg_lo:[1,0] neg_hi:[1,0]
	v_pk_add_f32 v[4:5], v[4:5], 1.0 op_sel_hi:[1,0]
	v_pk_mul_f32 v[10:11], v[10:11], v[14:15]
	v_rcp_f32_e32 v0, v0
	v_rcp_f32_e32 v1, v1
	v_pk_mul_f32 v[4:5], v[12:13], v[4:5]
	v_pk_add_f32 v[2:3], v[2:3], 1.0 op_sel_hi:[1,0]
	v_pk_add_f32 v[14:15], v[6:7], 1.0 op_sel_hi:[1,0] neg_lo:[1,0] neg_hi:[1,0]
	v_pk_add_f32 v[6:7], v[6:7], 1.0 op_sel_hi:[1,0]
	v_sqrt_f32_e32 v4, v4
	v_sqrt_f32_e32 v5, v5
	v_rcp_f32_e32 v2, v2
	v_rcp_f32_e32 v3, v3
	v_pk_mul_f32 v[6:7], v[14:15], v[6:7]
	v_lshlrev_b32_e32 v20, 16, v98
	v_sqrt_f32_e32 v6, v6
	v_sqrt_f32_e32 v7, v7
	v_and_b32_e32 v21, 0xffff0000, v98
	v_lshlrev_b32_e32 v22, 16, v99
	v_and_b32_e32 v23, 0xffff0000, v99
	v_pk_mul_f32 v[0:1], v[0:1], v[20:21]
	s_nop 0
	v_pk_mul_f32 v[4:5], v[0:1], v[4:5]
	v_pk_mul_f32 v[0:1], v[2:3], v[22:23]
	v_cvt_pk_bf16_f32 v2, v12, v13
	v_add_co_u32_e32 v12, vcc, 0x160000, v158
	v_pk_mul_f32 v[6:7], v[0:1], v[6:7]
	v_cvt_pk_bf16_f32 v0, v24, v25
	v_cvt_pk_bf16_f32 v1, v16, v17
	v_cvt_pk_bf16_f32 v3, v14, v15
	s_nop 0
	v_addc_co_u32_e32 v13, vcc, 0, v159, vcc
	global_store_dwordx4 v[12:13], v[0:3], off
	s_nop 1
	v_cvt_pk_bf16_f32 v0, v8, v9
	v_cvt_pk_bf16_f32 v1, v10, v11
	v_cvt_pk_bf16_f32 v2, v4, v5
	v_cvt_pk_bf16_f32 v3, v6, v7
	global_store_dwordx4 v[12:13], v[0:3], off offset:256
	s_and_b64 vcc, exec, s[6:7]
	s_mov_b64 s[6:7], -1
	s_cbranch_vccnz .LBB0_1268
	s_andn2_b64 vcc, exec, s[14:15]
	s_cbranch_vccnz .LBB0_1267
	s_barrier
	s_branch .LBB0_1267
